# speedup vs baseline: 1.1651x; 1.0036x over previous
_Z6conv_kILi256ELi512ELi3ELi128ELi1ELi1ELb0EEvPKDF16_S1_PKfS3_PDF16_S4_S1_fS3_S3_S3_S3_:
	s_lshl_b32 s3, s2, 3
	s_load_dwordx2 s[36:37], s[0:1], 0x0
	s_load_dwordx4 s[4:7], s[0:1], 0x10
	s_load_dwordx2 s[30:31], s[0:1], 0x30
	s_and_b32 s3, s3, 56
	s_ashr_i32 s8, s2, 5
	s_add_i32 s3, s3, s8
	v_readfirstlane_b32 s40, v0
	s_lshl_b32 s8, s3, 2
	s_bfe_u32 s49, s2, 0x20003
	s_and_b32 s33, s8, 56
	s_lshr_b32 s50, s40, 6
	s_bfe_u32 s41, s40, 0x10006
	s_ashr_i32 s38, s3, 4
	s_and_b32 s27, s2, 32
	s_lshl_b32 s2, s49, 9
	s_waitcnt lgkmcnt(0)
	s_add_u32 s2, s4, s2
	s_addc_u32 s3, s5, 0
	s_lshl_b32 s4, s41, 8
	s_add_u32 s2, s2, s4
	s_addc_u32 s3, s3, 0
	v_and_b32_e32 v18, 48, v0
	v_mov_b32_e32 v19, 0
	v_lshl_add_u64 v[2:3], s[2:3], 0, v[18:19]
	s_load_dword s26, s[6:7], 0x0
	global_load_dwordx4 v[14:17], v[2:3], off
	v_lshl_add_u64 v[4:5], v[2:3], 0, 64
	s_mov_b64 s[2:3], 0x80
	v_bfe_u32 v28, v0, 3, 3
	v_and_b32_e32 v1, 7, v0
	global_load_dwordx4 v[10:13], v[4:5], off
	v_lshl_add_u64 v[4:5], v[2:3], 0, s[2:3]
	s_mov_b64 s[2:3], 0xc0
	v_bitop3_b32 v1, v28, v1, 6 bitop3:0x6c
	v_lshl_add_u64 v[2:3], v[2:3], 0, s[2:3]
	v_lshl_or_b32 v18, s50, 3, v28
	s_mov_b32 s2, 0x1e1e1e1f
	v_lshlrev_b32_e32 v20, 3, v1
	v_mul_hi_u32 v1, v18, s2
	v_lshrrev_b32_e32 v21, 2, v1
	s_movk_i32 s8, 0xffde
	s_add_i32 s24, s33, -1
	global_load_dwordx4 v[6:9], v[4:5], off
	v_mul_lo_u32 v22, v21, s8
	v_add_u32_e32 v1, s24, v21
	s_add_i32 s25, s27, -1
	s_movk_i32 s9, 0x154
	global_load_dwordx4 v[2:5], v[2:3], off
	v_add3_u32 v24, s25, v18, v22
	v_cmp_gt_u32_e64 s[2:3], s9, v18
	v_cmp_gt_u32_e32 vcc, 64, v1
	s_and_b64 s[6:7], s[2:3], vcc
	v_cmp_gt_u32_e64 s[4:5], 64, v24
	v_and_b32_e32 v25, 63, v0
	s_and_b64 s[10:11], s[6:7], s[4:5]
	v_mov_b64_e32 v[22:23], s[30:31]
	v_lshlrev_b32_e32 v18, 1, v20
	s_and_saveexec_b64 s[6:7], s[10:11]
	s_lshl_b32 s10, s38, 14
	v_lshlrev_b32_e32 v1, 6, v1
	v_or3_b32 v22, v1, s10, v24
	v_ashrrev_i32_e32 v23, 31, v22
	v_lshlrev_b64 v[22:23], 7, v[22:23]
	v_lshl_add_u64 v[22:23], s[36:37], 0, v[22:23]
	v_lshl_add_u64 v[22:23], v[22:23], 0, v[18:19]
	s_or_b64 exec, exec, s[6:7]
	s_lshl_b32 s42, s50, 10
	v_lshlrev_b32_e32 v1, 4, v25
	v_or_b32_e32 v19, s42, v1
	s_add_i32 s13, s50, 8
	v_readfirstlane_b32 s6, v19
	s_mov_b32 m0, s6
	s_mov_b32 s12, 0x3c3c3c3d
	global_load_lds_dwordx4 v[22:23], off
	v_lshl_or_b32 v22, s13, 3, v28
	v_mul_hi_u32 v19, v22, s12
	v_lshrrev_b32_e32 v26, 3, v19
	v_mul_lo_u32 v23, v26, s8
	v_add_u32_e32 v19, s24, v26
	v_add3_u32 v27, s25, v22, v23
	v_cmp_gt_u32_e64 s[6:7], s9, v22
	v_cmp_gt_u32_e32 vcc, 64, v19
	s_and_b64 s[10:11], s[6:7], vcc
	v_cmp_gt_u32_e64 s[8:9], 64, v27
	s_and_b64 s[14:15], s[10:11], s[8:9]
	v_mov_b64_e32 v[22:23], s[30:31]
	s_and_saveexec_b64 s[10:11], s[14:15]
	s_lshl_b32 s14, s38, 14
	v_lshlrev_b32_e32 v19, 6, v19
	v_or3_b32 v22, v19, s14, v27
	v_ashrrev_i32_e32 v23, 31, v22
	v_lshlrev_b64 v[22:23], 7, v[22:23]
	v_lshl_add_u64 v[22:23], s[36:37], 0, v[22:23]
	v_mov_b32_e32 v19, 0
	v_lshl_add_u64 v[22:23], v[22:23], 0, v[18:19]
	s_or_b64 exec, exec, s[10:11]
	s_lshl_b32 s43, s13, 10
	v_or_b32_e32 v19, s43, v1
	s_add_i32 s18, s50, 16
	v_readfirstlane_b32 s10, v19
	s_mov_b32 m0, s10
	s_movk_i32 s16, 0xffde
	global_load_lds_dwordx4 v[22:23], off
	v_lshl_or_b32 v22, s18, 3, v28
	v_mul_hi_u32 v19, v22, s12
	v_lshrrev_b32_e32 v29, 3, v19
	v_mul_lo_u32 v23, v29, s16
	v_add_u32_e32 v19, s24, v29
	s_movk_i32 s17, 0x154
	v_add3_u32 v30, s25, v22, v23
	v_cmp_gt_u32_e64 s[10:11], s17, v22
	v_cmp_gt_u32_e32 vcc, 64, v19
	s_and_b64 s[14:15], s[10:11], vcc
	v_cmp_gt_u32_e64 s[12:13], 64, v30
	s_and_b64 s[20:21], s[14:15], s[12:13]
	v_mov_b64_e32 v[22:23], s[30:31]
	s_and_saveexec_b64 s[14:15], s[20:21]
	s_lshl_b32 s19, s38, 14
	v_lshlrev_b32_e32 v19, 6, v19
	v_or3_b32 v22, v19, s19, v30
	v_ashrrev_i32_e32 v23, 31, v22
	v_lshlrev_b64 v[22:23], 7, v[22:23]
	v_lshl_add_u64 v[22:23], s[36:37], 0, v[22:23]
	v_mov_b32_e32 v19, 0
	v_lshl_add_u64 v[22:23], v[22:23], 0, v[18:19]
	s_or_b64 exec, exec, s[14:15]
	s_lshl_b32 s44, s18, 10
	v_or_b32_e32 v19, s44, v1
	s_add_i32 s21, s50, 24
	v_readfirstlane_b32 s14, v19
	s_mov_b32 m0, s14
	s_mov_b32 s20, 0x3c3c3c3d
	global_load_lds_dwordx4 v[22:23], off
	v_lshl_or_b32 v22, s21, 3, v28
	v_mul_hi_u32 v19, v22, s20
	v_lshrrev_b32_e32 v31, 3, v19
	v_mul_lo_u32 v23, v31, s16
	v_add_u32_e32 v19, s24, v31
	v_add3_u32 v32, s25, v22, v23
	v_cmp_gt_u32_e64 s[14:15], s17, v22
	v_cmp_gt_u32_e32 vcc, 64, v19
	s_and_b64 s[18:19], s[14:15], vcc
	v_cmp_gt_u32_e64 s[16:17], 64, v32
	s_and_b64 s[22:23], s[18:19], s[16:17]
	v_mov_b64_e32 v[22:23], s[30:31]
	s_and_saveexec_b64 s[18:19], s[22:23]
	s_lshl_b32 s22, s38, 14
	v_lshlrev_b32_e32 v19, 6, v19
	v_or3_b32 v22, v19, s22, v32
	v_ashrrev_i32_e32 v23, 31, v22
	v_lshlrev_b64 v[22:23], 7, v[22:23]
	v_lshl_add_u64 v[22:23], s[36:37], 0, v[22:23]
	v_mov_b32_e32 v19, 0
	v_lshl_add_u64 v[22:23], v[22:23], 0, v[18:19]
	s_or_b64 exec, exec, s[18:19]
	s_lshl_b32 s45, s21, 10
	v_or_b32_e32 v19, s45, v1
	s_add_i32 s28, s50, 32
	v_readfirstlane_b32 s18, v19
	s_mov_b32 m0, s18
	s_movk_i32 s18, 0xffde
	global_load_lds_dwordx4 v[22:23], off
	v_lshl_or_b32 v22, s28, 3, v28
	v_mul_hi_u32 v19, v22, s20
	v_lshrrev_b32_e32 v33, 3, v19
	v_mul_lo_u32 v23, v33, s18
	v_add_u32_e32 v19, s24, v33
	s_movk_i32 s18, 0x154
	v_add3_u32 v34, s25, v22, v23
	v_cmp_gt_u32_e64 s[18:19], s18, v22
	v_cmp_gt_u32_e32 vcc, 64, v19
	s_and_b64 s[22:23], s[18:19], vcc
	v_cmp_gt_u32_e64 s[20:21], 64, v34
	s_and_b64 s[22:23], s[22:23], s[20:21]
	s_xor_b64 s[22:23], s[22:23], -1
	s_and_saveexec_b64 s[34:35], s[22:23]
	s_xor_b64 s[22:23], exec, s[34:35]
	s_lshl_b32 s29, s38, 14
	s_or_saveexec_b64 s[22:23], s[22:23]
	v_mov_b32_e32 v35, s29
	v_mov_b64_e32 v[22:23], s[30:31]
	s_xor_b64 exec, exec, s[22:23]
	s_lshl_b32 s29, s38, 14
	v_lshlrev_b32_e32 v19, 6, v19
	v_or3_b32 v22, v19, s29, v34
	v_ashrrev_i32_e32 v23, 31, v22
	v_lshlrev_b64 v[22:23], 7, v[22:23]
	v_lshl_add_u64 v[22:23], s[36:37], 0, v[22:23]
	v_mov_b32_e32 v19, 0
	v_lshl_add_u64 v[22:23], v[22:23], 0, v[18:19]
	v_mov_b32_e32 v35, s29
	s_or_b64 exec, exec, s[22:23]
	s_lshl_b32 s46, s28, 10
	v_or_b32_e32 v18, s46, v1
	s_add_i32 s48, s50, 40
	v_readfirstlane_b32 s22, v18
	s_mov_b32 m0, s22
	v_lshl_or_b32 v19, s48, 3, v28
	global_load_lds_dwordx4 v[22:23], off
	s_mov_b32 s22, 0x3c3c3c3d
	v_mul_hi_u32 v18, v19, s22
	v_lshrrev_b32_e32 v36, 3, v18
	s_movk_i32 s22, 0xffde
	s_load_dwordx2 s[34:35], s[0:1], 0x8
	v_mul_lo_u32 v22, v36, s22
	v_add_u32_e32 v18, s24, v36
	s_movk_i32 s22, 0x154
	v_add3_u32 v37, s25, v19, v22
	v_cmp_gt_u32_e64 s[22:23], s22, v19
	v_cmp_gt_u32_e32 vcc, 64, v18
	s_and_b64 s[28:29], s[22:23], vcc
	v_cmp_gt_u32_e64 s[24:25], 64, v37
	s_and_b64 s[28:29], s[28:29], s[24:25]
	s_xor_b64 s[28:29], s[28:29], -1
	s_and_saveexec_b64 s[52:53], s[28:29]
	s_xor_b64 s[28:29], exec, s[52:53]
	s_or_saveexec_b64 s[28:29], s[28:29]
	s_lshl_b32 s51, s41, 6
	v_mov_b64_e32 v[22:23], s[30:31]
	s_xor_b64 exec, exec, s[28:29]
	v_lshlrev_b32_e32 v18, 6, v18
	v_or3_b32 v18, v18, v35, v37
	v_ashrrev_i32_e32 v19, 31, v18
	v_lshlrev_b64 v[18:19], 7, v[18:19]
	v_lshl_add_u64 v[18:19], s[36:37], 0, v[18:19]
	v_lshlrev_b32_e32 v22, 1, v20
	v_mov_b32_e32 v23, 0
	v_lshl_add_u64 v[22:23], v[18:19], 0, v[22:23]
	s_or_b64 exec, exec, s[28:29]
	v_and_b32_e32 v114, 15, v0
	s_and_b32 s52, s50, 6
	v_mad_u64_u32 v[116:117], s[52:53], s52, 34, v[114:115]
	v_lshrrev_b32_e32 v115, 4, v25
	v_or_b32_e32 v19, s51, v114
	v_bitop3_b32 v25, v115, v0, 6 bitop3:0x78
	v_lshlrev_b32_e32 v19, 7, v19
	v_lshlrev_b32_e32 v25, 4, v25
	s_mov_b32 s51, 0x18040
	s_lshl_b32 s48, s48, 10
	v_lshlrev_b32_e32 v18, 6, v28
	v_or_b32_e32 v28, v19, v25
	v_bitop3_b32 v125, v19, s51, v25 bitop3:0x36
	v_or_b32_e32 v19, s48, v1
	s_lshl_b32 s39, s49, 7
	v_readfirstlane_b32 s51, v19
	s_lshr_b32 s47, s40, 7
	s_mov_b32 m0, s51
	s_lshl_b32 s51, s49, 14
	s_waitcnt lgkmcnt(0)
	s_add_u32 s52, s34, s51
	v_or3_b32 v18, s42, v18, v20
	s_addc_u32 s53, s35, 0
	s_lshl_b32 s56, s50, 11
	v_mov_b32_e32 v19, 0
	global_load_lds_dwordx4 v[22:23], off
	s_add_i32 s50, s56, 0x18000
	v_lshlrev_b64 v[22:23], 1, v[18:19]
	v_lshl_add_u64 v[118:119], s[52:53], 0, v[22:23]
	s_mov_b32 m0, s50
	s_mov_b64 s[34:35], 0x400
	global_load_lds_dwordx4 v[118:119], off
	s_add_i32 m0, s56, 0x18400
	s_add_u32 s54, s52, 0x30000
	v_lshl_add_u64 v[40:41], v[118:119], 0, s[34:35]
	s_addc_u32 s55, s53, 0
	global_load_lds_dwordx4 v[40:41], off
	s_add_i32 m0, s56, 0x1c000
	v_lshl_add_u64 v[40:41], s[54:55], 0, v[22:23]
	v_or_b32_e32 v38, 0x200, v18
	v_mov_b32_e32 v39, v19
	global_load_lds_dwordx4 v[40:41], off
	s_add_i32 m0, s56, 0x1c400
	v_lshlrev_b64 v[38:39], 1, v[38:39]
	s_add_u32 s52, s52, 0x60000
	v_lshl_add_u64 v[40:41], s[54:55], 0, v[38:39]
	s_addc_u32 s53, s53, 0
	global_load_lds_dwordx4 v[40:41], off
	s_add_i32 m0, s56, 0x20000
	v_lshl_add_u64 v[22:23], s[52:53], 0, v[22:23]
	global_load_lds_dwordx4 v[22:23], off
	v_lshl_add_u64 v[22:23], s[52:53], 0, v[38:39]
	s_add_i32 m0, s56, 0x20400
	v_or_b32_e32 v124, 0x18000, v28
	global_load_lds_dwordx4 v[22:23], off
	s_waitcnt vmcnt(4) lgkmcnt(0)
	s_barrier
	ds_read_b128 v[66:69], v124
	ds_read_b128 v[70:73], v124 offset:2048
	v_lshlrev_b32_e32 v18, 7, v116
	v_bitop3_b32 v22, v116, v115, 6 bitop3:0x6c
	v_add_u32_e32 v117, 34, v116
	v_lshl_or_b32 v138, v22, 4, v18
	ds_read_b128 v[78:81], v138
	ds_read_b128 v[74:77], v138 offset:2048
	v_lshlrev_b32_e32 v18, 7, v117
	v_bitop3_b32 v22, v117, v115, 6 bitop3:0x6c
	v_lshl_or_b32 v139, v22, 4, v18
	ds_read_b128 v[82:85], v139
	s_load_dwordx2 s[28:29], s[0:1], 0x20
	ds_read_b128 v[86:89], v139 offset:2048
	ds_read_b128 v[94:97], v124 offset:4096
	ds_read_b128 v[98:101], v124 offset:6144
	v_lshlrev_b32_e32 v18, 1, v20
	s_mov_b32 s49, 0
	s_mov_b32 s51, 1
	v_add_u32_e32 v126, s33, v21
	v_add_u32_e32 v127, v35, v24
	v_lshl_add_u64 v[120:121], s[36:37], 0, v[18:19]
	v_add_u32_e32 v128, s33, v26
	v_add_u32_e32 v129, v35, v27
	v_add_u32_e32 v130, s33, v29
	v_add_u32_e32 v131, v35, v30
	v_add_u32_e32 v132, s33, v31
	v_add_u32_e32 v133, v35, v32
	v_add_u32_e32 v134, s33, v33
	v_add_u32_e32 v135, v35, v34
	v_add_u32_e32 v136, s33, v36
	v_add_u32_e32 v137, v35, v37
	s_mov_b64 s[36:37], 0
	s_mov_b32 s52, 0
	v_mov_b32_e32 v18, v19
	v_mov_b32_e32 v20, v19
	v_mov_b32_e32 v21, v19
	v_mov_b32_e32 v38, v19
	v_mov_b32_e32 v39, v19
	v_mov_b32_e32 v40, v19
	v_mov_b32_e32 v41, v19
	v_mov_b32_e32 v42, v19
	v_mov_b32_e32 v43, v19
	v_mov_b32_e32 v44, v19
	v_mov_b32_e32 v45, v19
	v_mov_b32_e32 v46, v19
	v_mov_b32_e32 v47, v19
	v_mov_b32_e32 v48, v19
	v_mov_b32_e32 v49, v19
	v_mov_b32_e32 v50, v19
	v_mov_b32_e32 v51, v19
	v_mov_b32_e32 v52, v19
	v_mov_b32_e32 v53, v19
	v_mov_b32_e32 v54, v19
	v_mov_b32_e32 v55, v19
	v_mov_b32_e32 v56, v19
	v_mov_b32_e32 v57, v19
	v_mov_b32_e32 v58, v19
	v_mov_b32_e32 v59, v19
	v_mov_b32_e32 v60, v19
	v_mov_b32_e32 v61, v19
	v_mov_b32_e32 v62, v19
	v_mov_b32_e32 v63, v19
	v_mov_b32_e32 v64, v19
	v_mov_b32_e32 v65, v19
	v_mov_b32_e32 v90, v19
	v_mov_b32_e32 v91, v19
	v_mov_b32_e32 v92, v19
	v_mov_b32_e32 v93, v19
	v_mov_b32_e32 v102, v19
	v_mov_b32_e32 v103, v19
	v_mov_b32_e32 v104, v19
	v_mov_b32_e32 v105, v19
	v_mov_b32_e32 v106, v19
	v_mov_b32_e32 v107, v19
	v_mov_b32_e32 v108, v19
	v_mov_b32_e32 v109, v19
	v_mov_b32_e32 v110, v19
	v_mov_b32_e32 v111, v19
	v_mov_b32_e32 v112, v19
	v_mov_b32_e32 v113, v19
	v_mov_b32_e32 v34, v19
	v_mov_b32_e32 v35, v19
	v_mov_b32_e32 v36, v19
	v_mov_b32_e32 v37, v19
	v_mov_b32_e32 v30, v19
	v_mov_b32_e32 v31, v19
	v_mov_b32_e32 v32, v19
	v_mov_b32_e32 v33, v19
	v_mov_b32_e32 v26, v19
	v_mov_b32_e32 v27, v19
	v_mov_b32_e32 v28, v19
	v_mov_b32_e32 v29, v19
	v_mov_b32_e32 v22, v19
	v_mov_b32_e32 v23, v19
	v_mov_b32_e32 v24, v19
	v_mov_b32_e32 v25, v19
	s_mov_b32 s60, 0
	s_mov_b32 s61, 0
	s_mov_b32 s62, 0
	s_mov_b32 s64, 0
	s_mov_b32 s66, 1
	s_mov_b32 s67, 0
	s_mov_b32 s69, 0
	v_mov_b32_e32 v172, v125
	s_waitcnt lgkmcnt(0)

.Lc3_bar_0:
	s_barrier
	s_waitcnt lgkmcnt(3)
	v_mfma_f32_16x16x32_f16 v[110:113], v[66:69], v[78:81], v[110:113]
	ds_read_b128 v[140:143], v172
	v_mfma_f32_16x16x32_f16 v[106:109], v[70:73], v[78:81], v[106:109]
	v_xor_b32_e32 v174, 64, v139
	s_cmp_eq_u32 s61, 2
	s_cselect_b32 s79, 6, 0
	s_add_i32 s79, s79, s62
	s_add_i32 s79, s79, 1
	s_lshl_b32 s68, s79, 16
	s_waitcnt lgkmcnt(3)
	v_mfma_f32_16x16x32_f16 v[62:65], v[66:69], v[74:77], v[62:65]
	ds_read_b128 v[144:147], v172 offset:2048
	v_lshl_add_u64 v[176:177], v[118:119], 0, s[68:69]
	s_add_i32 s70, s49, 0xc000
	s_and_b32 s70, s70, 0xc000
	s_add_i32 s70, s70, s50
	v_mfma_f32_16x16x32_f16 v[58:61], v[70:73], v[74:77], v[58:61]
	v_xor_b32_e32 v175, 64, v138
	s_mov_b32 m0, s70
	s_add_i32 s71, s49, 0x4000
	global_load_lds_dwordx4 v[176:177], off
	v_mfma_f32_16x16x32_f16 v[46:49], v[66:69], v[82:85], v[46:49]
	ds_read_b128 v[156:159], v174
	v_mfma_f32_16x16x32_f16 v[42:45], v[70:73], v[82:85], v[42:45]
	s_and_b32 s71, s71, 0xc000
	s_add_i32 s72, s70, 0x400
	v_lshl_add_u64 v[178:179], v[176:177], 0, s[34:35]
	v_mfma_f32_16x16x32_f16 v[34:37], v[66:69], v[86:89], v[34:37]
	ds_read_b128 v[160:163], v174 offset:2048
	v_mfma_f32_16x16x32_f16 v[30:33], v[70:73], v[86:89], v[30:33]
	v_add_u32_e32 v173, s71, v124
	s_mov_b32 s76, s61
	s_mov_b32 s77, s64
	s_waitcnt lgkmcnt(5)
	v_mfma_f32_16x16x32_f16 v[102:105], v[94:97], v[78:81], v[102:105]
	ds_read_b128 v[148:151], v175
	s_waitcnt lgkmcnt(5)
	v_mfma_f32_16x16x32_f16 v[90:93], v[98:101], v[78:81], v[90:93]
	s_add_i32 s78, s76, 68
	v_mfma_f32_16x16x32_f16 v[54:57], v[94:97], v[74:77], v[54:57]
	ds_read_b128 v[152:155], v175 offset:2048
	v_mfma_f32_16x16x32_f16 v[50:53], v[98:101], v[74:77], v[50:53]
	v_add_u32_e32 v180, s78, v116
	v_mfma_f32_16x16x32_f16 v[38:41], v[94:97], v[82:85], v[38:41]
	ds_read_b128 v[164:167], v172 offset:4096
	v_mfma_f32_16x16x32_f16 v[18:21], v[98:101], v[82:85], v[18:21]
	v_bitop3_b32 v181, v180, v115, 6 bitop3:0x6c
	v_lshl_add_u32 v180, v180, 7, s77
	v_mfma_f32_16x16x32_f16 v[26:29], v[94:97], v[86:89], v[26:29]
	ds_read_b128 v[168:171], v172 offset:6144
	v_mfma_f32_16x16x32_f16 v[22:25], v[98:101], v[86:89], v[22:25]
	v_lshl_or_b32 v139, v181, 4, v180
	v_add_u32_e32 v172, s71, v125
	s_waitcnt lgkmcnt(3)
	v_mfma_f32_16x16x32_f16 v[110:113], v[140:143], v[148:151], v[110:113]
	ds_read_b128 v[66:69], v173
	v_mfma_f32_16x16x32_f16 v[106:109], v[144:147], v[148:151], v[106:109]
	s_mov_b32 m0, s72
	s_addk_i32 s49, 0x4000
	global_load_lds_dwordx4 v[178:179], off
	s_waitcnt lgkmcnt(3)
	v_mfma_f32_16x16x32_f16 v[62:65], v[140:143], v[152:155], v[62:65]
	ds_read_b128 v[70:73], v173 offset:2048
	v_mfma_f32_16x16x32_f16 v[58:61], v[144:147], v[152:155], v[58:61]
	v_mfma_f32_16x16x32_f16 v[46:49], v[140:143], v[156:159], v[46:49]
	ds_read_b128 v[78:81], v139
	v_mfma_f32_16x16x32_f16 v[42:45], v[144:147], v[156:159], v[42:45]
	v_mfma_f32_16x16x32_f16 v[34:37], v[140:143], v[160:163], v[34:37]
	ds_read_b128 v[74:77], v139 offset:2048
	v_mfma_f32_16x16x32_f16 v[30:33], v[144:147], v[160:163], v[30:33]
	s_waitcnt lgkmcnt(5)
	v_mfma_f32_16x16x32_f16 v[102:105], v[164:167], v[148:151], v[102:105]
	s_waitcnt lgkmcnt(4)
	v_mfma_f32_16x16x32_f16 v[90:93], v[168:171], v[148:151], v[90:93]
	v_mfma_f32_16x16x32_f16 v[54:57], v[164:167], v[152:155], v[54:57]
	v_mfma_f32_16x16x32_f16 v[50:53], v[168:171], v[152:155], v[50:53]
	s_add_i32 s60, s60, 1
	v_mfma_f32_16x16x32_f16 v[38:41], v[164:167], v[156:159], v[38:41]
	ds_read_b128 v[94:97], v173 offset:4096
	v_mfma_f32_16x16x32_f16 v[18:21], v[168:171], v[156:159], v[18:21]
	v_mfma_f32_16x16x32_f16 v[26:29], v[164:167], v[160:163], v[26:29]
	ds_read_b128 v[98:101], v173 offset:6144
	v_mfma_f32_16x16x32_f16 v[22:25], v[168:171], v[160:163], v[22:25]
	s_cmp_lg_u32 s60, s66
	s_cbranch_scc1 .Lc3_np0
	s_ashr_i32 s36, s51, 31
	s_lshr_b32 s36, s36, 30
	s_add_i32 s36, s51, s36
	s_ashr_i32 s36, s36, 2
	s_mul_i32 s54, s36, 3
	s_add_i32 s54, s54, -1
	v_add_u32_e32 v140, s54, v126
	s_lshl_b32 s37, s51, 6
	s_lshl_b32 s36, s36, 8
	v_cmp_gt_u32_e32 vcc, 64, v140
	s_sub_i32 s53, s37, s36
	s_and_b64 s[36:37], s[2:3], vcc
	s_and_b64 s[56:57], s[36:37], s[4:5]
	v_mov_b64_e32 v[122:123], s[30:31]
	s_and_saveexec_b64 s[36:37], s[56:57]
	v_or_b32_e32 v122, s53, v140
	v_lshl_add_u32 v122, v122, 6, v127
	v_ashrrev_i32_e32 v123, 31, v122
	v_lshlrev_b64 v[122:123], 7, v[122:123]
	v_lshl_add_u64 v[122:123], v[120:121], 0, v[122:123]
	s_or_b64 exec, exec, s[36:37]
	s_bitcmp1_b32 s51, 0
	s_cselect_b32 s55, 0xc000, 0
	s_add_i32 s36, s55, s42
	v_add_u32_e32 v140, s36, v1
	s_nop 0
	v_readfirstlane_b32 s36, v140
	s_mov_b32 m0, s36
	v_add_u32_e32 v140, s54, v128
	global_load_lds_dwordx4 v[122:123], off
	v_cmp_gt_u32_e32 vcc, 64, v140
	s_and_b64 s[36:37], s[6:7], vcc
	s_and_b64 s[56:57], s[36:37], s[8:9]
	v_mov_b64_e32 v[122:123], s[30:31]
	s_and_saveexec_b64 s[36:37], s[56:57]
	v_or_b32_e32 v122, s53, v140
	v_lshl_add_u32 v122, v122, 6, v129
	v_ashrrev_i32_e32 v123, 31, v122
	v_lshlrev_b64 v[122:123], 7, v[122:123]
	v_lshl_add_u64 v[122:123], v[120:121], 0, v[122:123]
	s_or_b64 exec, exec, s[36:37]
	s_add_i32 s36, s55, s43
	v_add_u32_e32 v140, s36, v1
	s_nop 0
	v_readfirstlane_b32 s36, v140
	s_mov_b32 m0, s36
	v_add_u32_e32 v140, s54, v130
	global_load_lds_dwordx4 v[122:123], off
	v_cmp_gt_u32_e32 vcc, 64, v140
	s_and_b64 s[36:37], s[10:11], vcc
	s_and_b64 s[56:57], s[36:37], s[12:13]
	v_mov_b64_e32 v[122:123], s[30:31]
	s_and_saveexec_b64 s[36:37], s[56:57]
	v_or_b32_e32 v122, s53, v140
	v_lshl_add_u32 v122, v122, 6, v131
	v_ashrrev_i32_e32 v123, 31, v122
	v_lshlrev_b64 v[122:123], 7, v[122:123]
	v_lshl_add_u64 v[122:123], v[120:121], 0, v[122:123]
	s_or_b64 exec, exec, s[36:37]
	s_add_i32 s36, s55, s44
	v_add_u32_e32 v140, s36, v1
	s_nop 0
	v_readfirstlane_b32 s36, v140
	s_mov_b32 m0, s36
	v_add_u32_e32 v140, s54, v132
	global_load_lds_dwordx4 v[122:123], off
	v_cmp_gt_u32_e32 vcc, 64, v140
	s_and_b64 s[36:37], s[14:15], vcc
	s_and_b64 s[56:57], s[36:37], s[16:17]
	v_mov_b64_e32 v[122:123], s[30:31]
	s_and_saveexec_b64 s[36:37], s[56:57]
	v_or_b32_e32 v122, s53, v140
	v_lshl_add_u32 v122, v122, 6, v133
	v_ashrrev_i32_e32 v123, 31, v122
	v_lshlrev_b64 v[122:123], 7, v[122:123]
	v_lshl_add_u64 v[122:123], v[120:121], 0, v[122:123]
	s_or_b64 exec, exec, s[36:37]
	s_add_i32 s36, s55, s45
	v_add_u32_e32 v140, s36, v1
	s_nop 0
	v_readfirstlane_b32 s36, v140
	s_mov_b32 m0, s36
	v_add_u32_e32 v140, s54, v134
	global_load_lds_dwordx4 v[122:123], off
	v_cmp_gt_u32_e32 vcc, 64, v140
	s_and_b64 s[36:37], s[18:19], vcc
	s_and_b64 s[56:57], s[36:37], s[20:21]
	v_mov_b64_e32 v[122:123], s[30:31]
	s_and_saveexec_b64 s[36:37], s[56:57]
	v_or_b32_e32 v122, s53, v140
	v_lshl_add_u32 v122, v122, 6, v135
	v_ashrrev_i32_e32 v123, 31, v122
	v_lshlrev_b64 v[122:123], 7, v[122:123]
	v_lshl_add_u64 v[122:123], v[120:121], 0, v[122:123]
	s_or_b64 exec, exec, s[36:37]
	s_add_i32 s36, s55, s46
	v_add_u32_e32 v140, s36, v1
	s_nop 0
	v_readfirstlane_b32 s36, v140
	s_mov_b32 m0, s36
	v_add_u32_e32 v140, s54, v136
	global_load_lds_dwordx4 v[122:123], off
	v_cmp_gt_u32_e32 vcc, 64, v140
	s_and_b64 s[36:37], s[22:23], vcc
	s_and_b64 s[56:57], s[36:37], s[24:25]
	v_mov_b64_e32 v[122:123], s[30:31]
	s_and_saveexec_b64 s[36:37], s[56:57]
	s_cbranch_execz .Lc3_ptail0
	v_or_b32_e32 v122, s53, v140
	v_lshl_add_u32 v122, v122, 6, v137
	v_ashrrev_i32_e32 v123, 31, v122
	v_lshlrev_b64 v[122:123], 7, v[122:123]
	v_lshl_add_u64 v[122:123], v[120:121], 0, v[122:123]
	s_branch .Lc3_ptail0
.Lc3_ptail0:
	s_or_b64 exec, exec, s[36:37]
	s_add_i32 s55, s55, s48
	v_add_u32_e32 v140, s55, v1
	s_add_i32 s51, s51, 1
	v_readfirstlane_b32 s36, v140
	s_mov_b32 m0, s36
	s_mov_b64 s[36:37], -1
	global_load_lds_dwordx4 v[122:123], off
	s_add_i32 s66, s66, 9
	s_cmp_gt_u32 s51, 3
	s_cselect_b32 s66, 0x3e8, s66
	s_mov_b32 s67, 2
.Lc3_np0:
	s_cmp_eq_u32 s67, 0
	s_cbranch_scc1 .Lc3_w2_1
	s_waitcnt vmcnt(8)
	s_sub_i32 s67, s67, 1
	s_branch .Lc3_bar_1

.Lc3_bar_1:
	s_barrier
	s_waitcnt lgkmcnt(5)
	v_mfma_f32_16x16x32_f16 v[110:113], v[66:69], v[82:85], v[110:113]
	ds_read_b128 v[140:143], v172
	s_waitcnt lgkmcnt(5)
	v_mfma_f32_16x16x32_f16 v[106:109], v[70:73], v[82:85], v[106:109]
	v_xor_b32_e32 v174, 64, v139
	s_cmp_eq_u32 s61, 2
	s_cselect_b32 s79, 6, 0
	s_add_i32 s79, s79, s62
	s_add_i32 s79, s79, 4
	s_lshl_b32 s68, s79, 16
	v_mfma_f32_16x16x32_f16 v[62:65], v[66:69], v[86:89], v[62:65]
	ds_read_b128 v[144:147], v172 offset:2048
	v_lshl_add_u64 v[176:177], v[118:119], 0, s[68:69]
	s_add_i32 s70, s49, 0xc000
	s_and_b32 s70, s70, 0xc000
	s_add_i32 s70, s70, s50
	v_mfma_f32_16x16x32_f16 v[58:61], v[70:73], v[86:89], v[58:61]
	s_mov_b32 m0, s70
	s_add_i32 s71, s49, 0x4000
	global_load_lds_dwordx4 v[176:177], off
	s_waitcnt lgkmcnt(5)
	v_mfma_f32_16x16x32_f16 v[46:49], v[66:69], v[78:81], v[46:49]
	ds_read_b128 v[148:151], v174
	v_mfma_f32_16x16x32_f16 v[42:45], v[70:73], v[78:81], v[42:45]
	s_and_b32 s71, s71, 0xc000
	s_add_i32 s72, s70, 0x400
	v_lshl_add_u64 v[178:179], v[176:177], 0, s[34:35]
	s_waitcnt lgkmcnt(5)
	v_mfma_f32_16x16x32_f16 v[34:37], v[66:69], v[74:77], v[34:37]
	ds_read_b128 v[152:155], v174 offset:2048
	v_mfma_f32_16x16x32_f16 v[30:33], v[70:73], v[74:77], v[30:33]
	v_add_u32_e32 v173, s71, v124
	s_mov_b32 s76, s61
	s_mov_b32 s77, s64
	s_waitcnt lgkmcnt(5)
	v_mfma_f32_16x16x32_f16 v[102:105], v[94:97], v[82:85], v[102:105]
	s_waitcnt lgkmcnt(4)
	v_mfma_f32_16x16x32_f16 v[90:93], v[98:101], v[82:85], v[90:93]
	s_add_i32 s78, s76, 102
	v_mfma_f32_16x16x32_f16 v[54:57], v[94:97], v[86:89], v[54:57]
	v_mfma_f32_16x16x32_f16 v[50:53], v[98:101], v[86:89], v[50:53]
	v_add_u32_e32 v180, s78, v116
	v_mfma_f32_16x16x32_f16 v[38:41], v[94:97], v[78:81], v[38:41]
	ds_read_b128 v[164:167], v172 offset:4096
	v_mfma_f32_16x16x32_f16 v[18:21], v[98:101], v[78:81], v[18:21]
	v_bitop3_b32 v181, v180, v115, 6 bitop3:0x6c
	v_lshl_add_u32 v180, v180, 7, s77
	v_mfma_f32_16x16x32_f16 v[26:29], v[94:97], v[74:77], v[26:29]
	ds_read_b128 v[168:171], v172 offset:6144
	v_mfma_f32_16x16x32_f16 v[22:25], v[98:101], v[74:77], v[22:25]
	v_lshl_or_b32 v139, v181, 4, v180
	v_add_u32_e32 v172, s71, v125
	s_waitcnt lgkmcnt(5)
	v_mfma_f32_16x16x32_f16 v[110:113], v[140:143], v[156:159], v[110:113]
	ds_read_b128 v[66:69], v173
	s_waitcnt lgkmcnt(5)
	v_mfma_f32_16x16x32_f16 v[106:109], v[144:147], v[156:159], v[106:109]
	s_mov_b32 m0, s72
	s_addk_i32 s49, 0x4000
	global_load_lds_dwordx4 v[178:179], off
	v_mfma_f32_16x16x32_f16 v[62:65], v[140:143], v[160:163], v[62:65]
	ds_read_b128 v[70:73], v173 offset:2048
	v_mfma_f32_16x16x32_f16 v[58:61], v[144:147], v[160:163], v[58:61]
	s_waitcnt lgkmcnt(5)
	v_mfma_f32_16x16x32_f16 v[46:49], v[140:143], v[148:151], v[46:49]
	ds_read_b128 v[82:85], v139
	v_mfma_f32_16x16x32_f16 v[42:45], v[144:147], v[148:151], v[42:45]
	s_waitcnt lgkmcnt(5)
	v_mfma_f32_16x16x32_f16 v[34:37], v[140:143], v[152:155], v[34:37]
	ds_read_b128 v[86:89], v139 offset:2048
	v_mfma_f32_16x16x32_f16 v[30:33], v[144:147], v[152:155], v[30:33]
	s_waitcnt lgkmcnt(5)
	v_mfma_f32_16x16x32_f16 v[102:105], v[164:167], v[156:159], v[102:105]
	s_waitcnt lgkmcnt(4)
	v_mfma_f32_16x16x32_f16 v[90:93], v[168:171], v[156:159], v[90:93]
	v_mfma_f32_16x16x32_f16 v[54:57], v[164:167], v[160:163], v[54:57]
	v_mfma_f32_16x16x32_f16 v[50:53], v[168:171], v[160:163], v[50:53]
	s_add_i32 s60, s60, 1
	v_mfma_f32_16x16x32_f16 v[38:41], v[164:167], v[148:151], v[38:41]
	ds_read_b128 v[94:97], v173 offset:4096
	v_mfma_f32_16x16x32_f16 v[18:21], v[168:171], v[148:151], v[18:21]
	v_mfma_f32_16x16x32_f16 v[26:29], v[164:167], v[152:155], v[26:29]
	ds_read_b128 v[98:101], v173 offset:6144
	v_mfma_f32_16x16x32_f16 v[22:25], v[168:171], v[152:155], v[22:25]
	s_cmp_eq_u32 s67, 0
	s_cbranch_scc1 .Lc3_w2_2
	s_waitcnt vmcnt(8)
	s_sub_i32 s67, s67, 1
	s_branch .Lc3_bar_2

.Lc3_bar_2:
	s_barrier
	s_waitcnt lgkmcnt(5)
	v_mfma_f32_16x16x32_f16 v[110:113], v[66:69], v[78:81], v[110:113]
	ds_read_b128 v[140:143], v172
	s_waitcnt lgkmcnt(5)
	v_mfma_f32_16x16x32_f16 v[106:109], v[70:73], v[78:81], v[106:109]
	v_xor_b32_e32 v174, 64, v139
	s_cmp_eq_u32 s61, 2
	s_cselect_b32 s79, 6, 0
	s_add_i32 s79, s79, s62
	s_add_i32 s79, s79, 7
	s_lshl_b32 s68, s79, 16
	v_mfma_f32_16x16x32_f16 v[62:65], v[66:69], v[74:77], v[62:65]
	ds_read_b128 v[144:147], v172 offset:2048
	v_lshl_add_u64 v[176:177], v[118:119], 0, s[68:69]
	s_add_i32 s70, s49, 0xc000
	s_and_b32 s70, s70, 0xc000
	s_add_i32 s70, s70, s50
	v_mfma_f32_16x16x32_f16 v[58:61], v[70:73], v[74:77], v[58:61]
	s_mov_b32 m0, s70
	s_add_i32 s71, s49, 0x4000
	global_load_lds_dwordx4 v[176:177], off
	s_waitcnt lgkmcnt(5)
	v_mfma_f32_16x16x32_f16 v[46:49], v[66:69], v[82:85], v[46:49]
	ds_read_b128 v[156:159], v174
	v_mfma_f32_16x16x32_f16 v[42:45], v[70:73], v[82:85], v[42:45]
	s_and_b32 s71, s71, 0xc000
	s_add_i32 s72, s70, 0x400
	v_lshl_add_u64 v[178:179], v[176:177], 0, s[34:35]
	s_waitcnt lgkmcnt(5)
	v_mfma_f32_16x16x32_f16 v[34:37], v[66:69], v[86:89], v[34:37]
	ds_read_b128 v[160:163], v174 offset:2048
	v_mfma_f32_16x16x32_f16 v[30:33], v[70:73], v[86:89], v[30:33]
	v_add_u32_e32 v173, s71, v124
	s_add_i32 s76, s61, 1
	s_cmp_eq_u32 s61, 2
	s_cselect_b32 s76, 0, s76
	s_cselect_b32 s77, 0xc000, 0
	s_xor_b32 s77, s77, s64
	s_waitcnt lgkmcnt(5)
	v_mfma_f32_16x16x32_f16 v[102:105], v[94:97], v[78:81], v[102:105]
	s_waitcnt lgkmcnt(4)
	v_mfma_f32_16x16x32_f16 v[90:93], v[98:101], v[78:81], v[90:93]
	s_add_i32 s78, s76, 34
	v_mfma_f32_16x16x32_f16 v[54:57], v[94:97], v[74:77], v[54:57]
	v_mfma_f32_16x16x32_f16 v[50:53], v[98:101], v[74:77], v[50:53]
	v_add_u32_e32 v180, s78, v116
	v_mfma_f32_16x16x32_f16 v[38:41], v[94:97], v[82:85], v[38:41]
	ds_read_b128 v[164:167], v172 offset:4096
	v_mfma_f32_16x16x32_f16 v[18:21], v[98:101], v[82:85], v[18:21]
	v_bitop3_b32 v181, v180, v115, 6 bitop3:0x6c
	v_lshl_add_u32 v180, v180, 7, s77
	v_mfma_f32_16x16x32_f16 v[26:29], v[94:97], v[86:89], v[26:29]
	ds_read_b128 v[168:171], v172 offset:6144
	v_mfma_f32_16x16x32_f16 v[22:25], v[98:101], v[86:89], v[22:25]
	v_lshl_or_b32 v139, v181, 4, v180
	v_add_u32_e32 v172, s71, v125
	s_waitcnt lgkmcnt(5)
	v_mfma_f32_16x16x32_f16 v[110:113], v[140:143], v[148:151], v[110:113]
	ds_read_b128 v[66:69], v173
	s_waitcnt lgkmcnt(5)
	v_mfma_f32_16x16x32_f16 v[106:109], v[144:147], v[148:151], v[106:109]
	s_mov_b32 m0, s72
	s_addk_i32 s49, 0x4000
	global_load_lds_dwordx4 v[178:179], off
	v_mfma_f32_16x16x32_f16 v[62:65], v[140:143], v[152:155], v[62:65]
	ds_read_b128 v[70:73], v173 offset:2048
	v_mfma_f32_16x16x32_f16 v[58:61], v[144:147], v[152:155], v[58:61]
	s_sub_i32 s78, s78, 34
	v_add_u32_e32 v180, s78, v116
	s_waitcnt lgkmcnt(5)
	v_mfma_f32_16x16x32_f16 v[46:49], v[140:143], v[156:159], v[46:49]
	ds_read_b128 v[78:81], v139
	v_mfma_f32_16x16x32_f16 v[42:45], v[144:147], v[156:159], v[42:45]
	v_bitop3_b32 v181, v180, v115, 6 bitop3:0x6c
	v_lshl_add_u32 v180, v180, 7, s77
	s_waitcnt lgkmcnt(5)
	v_mfma_f32_16x16x32_f16 v[34:37], v[140:143], v[160:163], v[34:37]
	ds_read_b128 v[74:77], v139 offset:2048
	v_mfma_f32_16x16x32_f16 v[30:33], v[144:147], v[160:163], v[30:33]
	v_lshl_or_b32 v138, v181, 4, v180
	s_waitcnt lgkmcnt(5)
	v_mfma_f32_16x16x32_f16 v[102:105], v[164:167], v[148:151], v[102:105]
	ds_read_b128 v[82:85], v138
	s_waitcnt lgkmcnt(5)
	v_mfma_f32_16x16x32_f16 v[90:93], v[168:171], v[148:151], v[90:93]
	v_mfma_f32_16x16x32_f16 v[54:57], v[164:167], v[152:155], v[54:57]
	ds_read_b128 v[86:89], v138 offset:2048
	v_mfma_f32_16x16x32_f16 v[50:53], v[168:171], v[152:155], v[50:53]
	s_add_i32 s60, s60, 1
	s_cmp_eq_u32 s61, 2
	s_cselect_b32 s79, 7, 1
	s_add_i32 s62, s62, s79
	s_mov_b32 s61, s76
	s_mov_b32 s64, s77
	v_mfma_f32_16x16x32_f16 v[38:41], v[164:167], v[156:159], v[38:41]
	ds_read_b128 v[94:97], v173 offset:4096
	v_mfma_f32_16x16x32_f16 v[18:21], v[168:171], v[156:159], v[18:21]
	v_mfma_f32_16x16x32_f16 v[26:29], v[164:167], v[160:163], v[26:29]
	ds_read_b128 v[98:101], v173 offset:6144
	v_mfma_f32_16x16x32_f16 v[22:25], v[168:171], v[160:163], v[22:25]
	s_cmp_eq_u32 s67, 0
	s_cbranch_scc1 .Lc3_w2_3
	s_waitcnt vmcnt(8)
	s_sub_i32 s67, s67, 1
	s_branch .Lc3_bar_3

.Lc3_bar_3:
	s_barrier
	s_waitcnt lgkmcnt(3)
	v_mfma_f32_16x16x32_f16 v[110:113], v[66:69], v[82:85], v[110:113]
	ds_read_b128 v[140:143], v172
	v_mfma_f32_16x16x32_f16 v[106:109], v[70:73], v[82:85], v[106:109]
	v_xor_b32_e32 v174, 64, v139
	s_cmp_eq_u32 s61, 2
	s_cselect_b32 s79, 6, 0
	s_add_i32 s79, s79, s62
	s_add_i32 s79, s79, 1
	s_lshl_b32 s68, s79, 16
	s_waitcnt lgkmcnt(3)
	v_mfma_f32_16x16x32_f16 v[62:65], v[66:69], v[86:89], v[62:65]
	ds_read_b128 v[144:147], v172 offset:2048
	v_lshl_add_u64 v[176:177], v[118:119], 0, s[68:69]
	s_add_i32 s70, s49, 0xc000
	s_and_b32 s70, s70, 0xc000
	s_add_i32 s70, s70, s50
	v_mfma_f32_16x16x32_f16 v[58:61], v[70:73], v[86:89], v[58:61]
	v_xor_b32_e32 v175, 64, v138
	s_mov_b32 m0, s70
	s_add_i32 s71, s49, 0x4000
	global_load_lds_dwordx4 v[176:177], off
	v_mfma_f32_16x16x32_f16 v[46:49], v[66:69], v[78:81], v[46:49]
	ds_read_b128 v[148:151], v174
	v_mfma_f32_16x16x32_f16 v[42:45], v[70:73], v[78:81], v[42:45]
	s_and_b32 s71, s71, 0xc000
	s_add_i32 s72, s70, 0x400
	v_lshl_add_u64 v[178:179], v[176:177], 0, s[34:35]
	v_mfma_f32_16x16x32_f16 v[34:37], v[66:69], v[74:77], v[34:37]
	ds_read_b128 v[152:155], v174 offset:2048
	v_mfma_f32_16x16x32_f16 v[30:33], v[70:73], v[74:77], v[30:33]
	v_add_u32_e32 v173, s71, v124
	s_mov_b32 s76, s61
	s_mov_b32 s77, s64
	s_waitcnt lgkmcnt(5)
	v_mfma_f32_16x16x32_f16 v[102:105], v[94:97], v[82:85], v[102:105]
	ds_read_b128 v[156:159], v175
	s_waitcnt lgkmcnt(5)
	v_mfma_f32_16x16x32_f16 v[90:93], v[98:101], v[82:85], v[90:93]
	s_add_i32 s78, s76, 68
	v_mfma_f32_16x16x32_f16 v[54:57], v[94:97], v[86:89], v[54:57]
	ds_read_b128 v[160:163], v175 offset:2048
	v_mfma_f32_16x16x32_f16 v[50:53], v[98:101], v[86:89], v[50:53]
	v_add_u32_e32 v180, s78, v116
	v_mfma_f32_16x16x32_f16 v[38:41], v[94:97], v[78:81], v[38:41]
	ds_read_b128 v[164:167], v172 offset:4096
	v_mfma_f32_16x16x32_f16 v[18:21], v[98:101], v[78:81], v[18:21]
	v_bitop3_b32 v181, v180, v115, 6 bitop3:0x6c
	v_lshl_add_u32 v180, v180, 7, s77
	v_mfma_f32_16x16x32_f16 v[26:29], v[94:97], v[74:77], v[26:29]
	ds_read_b128 v[168:171], v172 offset:6144
	v_mfma_f32_16x16x32_f16 v[22:25], v[98:101], v[74:77], v[22:25]
	v_lshl_or_b32 v139, v181, 4, v180
	v_add_u32_e32 v172, s71, v125
	s_waitcnt lgkmcnt(3)
	v_mfma_f32_16x16x32_f16 v[110:113], v[140:143], v[156:159], v[110:113]
	ds_read_b128 v[66:69], v173
	v_mfma_f32_16x16x32_f16 v[106:109], v[144:147], v[156:159], v[106:109]
	s_mov_b32 m0, s72
	s_addk_i32 s49, 0x4000
	global_load_lds_dwordx4 v[178:179], off
	s_waitcnt lgkmcnt(3)
	v_mfma_f32_16x16x32_f16 v[62:65], v[140:143], v[160:163], v[62:65]
	ds_read_b128 v[70:73], v173 offset:2048
	v_mfma_f32_16x16x32_f16 v[58:61], v[144:147], v[160:163], v[58:61]
	v_mfma_f32_16x16x32_f16 v[46:49], v[140:143], v[148:151], v[46:49]
	ds_read_b128 v[82:85], v139
	v_mfma_f32_16x16x32_f16 v[42:45], v[144:147], v[148:151], v[42:45]
	v_mfma_f32_16x16x32_f16 v[34:37], v[140:143], v[152:155], v[34:37]
	ds_read_b128 v[86:89], v139 offset:2048
	v_mfma_f32_16x16x32_f16 v[30:33], v[144:147], v[152:155], v[30:33]
	s_waitcnt lgkmcnt(5)
	v_mfma_f32_16x16x32_f16 v[102:105], v[164:167], v[156:159], v[102:105]
	s_waitcnt lgkmcnt(4)
	v_mfma_f32_16x16x32_f16 v[90:93], v[168:171], v[156:159], v[90:93]
	v_mfma_f32_16x16x32_f16 v[54:57], v[164:167], v[160:163], v[54:57]
	v_mfma_f32_16x16x32_f16 v[50:53], v[168:171], v[160:163], v[50:53]
	s_add_i32 s60, s60, 1
	v_mfma_f32_16x16x32_f16 v[38:41], v[164:167], v[148:151], v[38:41]
	ds_read_b128 v[94:97], v173 offset:4096
	v_mfma_f32_16x16x32_f16 v[18:21], v[168:171], v[148:151], v[18:21]
	v_mfma_f32_16x16x32_f16 v[26:29], v[164:167], v[152:155], v[26:29]
	ds_read_b128 v[98:101], v173 offset:6144
	v_mfma_f32_16x16x32_f16 v[22:25], v[168:171], v[152:155], v[22:25]
	s_cmp_lg_u32 s60, s66
	s_cbranch_scc1 .Lc3_np3
	s_ashr_i32 s36, s51, 31
	s_lshr_b32 s36, s36, 30
	s_add_i32 s36, s51, s36
	s_ashr_i32 s36, s36, 2
	s_mul_i32 s54, s36, 3
	s_add_i32 s54, s54, -1
	v_add_u32_e32 v140, s54, v126
	s_lshl_b32 s37, s51, 6
	s_lshl_b32 s36, s36, 8
	v_cmp_gt_u32_e32 vcc, 64, v140
	s_sub_i32 s53, s37, s36
	s_and_b64 s[36:37], s[2:3], vcc
	s_and_b64 s[56:57], s[36:37], s[4:5]
	v_mov_b64_e32 v[122:123], s[30:31]
	s_and_saveexec_b64 s[36:37], s[56:57]
	v_or_b32_e32 v122, s53, v140
	v_lshl_add_u32 v122, v122, 6, v127
	v_ashrrev_i32_e32 v123, 31, v122
	v_lshlrev_b64 v[122:123], 7, v[122:123]
	v_lshl_add_u64 v[122:123], v[120:121], 0, v[122:123]
	s_or_b64 exec, exec, s[36:37]
	s_bitcmp1_b32 s51, 0
	s_cselect_b32 s55, 0xc000, 0
	s_add_i32 s36, s55, s42
	v_add_u32_e32 v140, s36, v1
	s_nop 0
	v_readfirstlane_b32 s36, v140
	s_mov_b32 m0, s36
	v_add_u32_e32 v140, s54, v128
	global_load_lds_dwordx4 v[122:123], off
	v_cmp_gt_u32_e32 vcc, 64, v140
	s_and_b64 s[36:37], s[6:7], vcc
	s_and_b64 s[56:57], s[36:37], s[8:9]
	v_mov_b64_e32 v[122:123], s[30:31]
	s_and_saveexec_b64 s[36:37], s[56:57]
	v_or_b32_e32 v122, s53, v140
	v_lshl_add_u32 v122, v122, 6, v129
	v_ashrrev_i32_e32 v123, 31, v122
	v_lshlrev_b64 v[122:123], 7, v[122:123]
	v_lshl_add_u64 v[122:123], v[120:121], 0, v[122:123]
	s_or_b64 exec, exec, s[36:37]
	s_add_i32 s36, s55, s43
	v_add_u32_e32 v140, s36, v1
	s_nop 0
	v_readfirstlane_b32 s36, v140
	s_mov_b32 m0, s36
	v_add_u32_e32 v140, s54, v130
	global_load_lds_dwordx4 v[122:123], off
	v_cmp_gt_u32_e32 vcc, 64, v140
	s_and_b64 s[36:37], s[10:11], vcc
	s_and_b64 s[56:57], s[36:37], s[12:13]
	v_mov_b64_e32 v[122:123], s[30:31]
	s_and_saveexec_b64 s[36:37], s[56:57]
	v_or_b32_e32 v122, s53, v140
	v_lshl_add_u32 v122, v122, 6, v131
	v_ashrrev_i32_e32 v123, 31, v122
	v_lshlrev_b64 v[122:123], 7, v[122:123]
	v_lshl_add_u64 v[122:123], v[120:121], 0, v[122:123]
	s_or_b64 exec, exec, s[36:37]
	s_add_i32 s36, s55, s44
	v_add_u32_e32 v140, s36, v1
	s_nop 0
	v_readfirstlane_b32 s36, v140
	s_mov_b32 m0, s36
	v_add_u32_e32 v140, s54, v132
	global_load_lds_dwordx4 v[122:123], off
	v_cmp_gt_u32_e32 vcc, 64, v140
	s_and_b64 s[36:37], s[14:15], vcc
	s_and_b64 s[56:57], s[36:37], s[16:17]
	v_mov_b64_e32 v[122:123], s[30:31]
	s_and_saveexec_b64 s[36:37], s[56:57]
	v_or_b32_e32 v122, s53, v140
	v_lshl_add_u32 v122, v122, 6, v133
	v_ashrrev_i32_e32 v123, 31, v122
	v_lshlrev_b64 v[122:123], 7, v[122:123]
	v_lshl_add_u64 v[122:123], v[120:121], 0, v[122:123]
	s_or_b64 exec, exec, s[36:37]
	s_add_i32 s36, s55, s45
	v_add_u32_e32 v140, s36, v1
	s_nop 0
	v_readfirstlane_b32 s36, v140
	s_mov_b32 m0, s36
	v_add_u32_e32 v140, s54, v134
	global_load_lds_dwordx4 v[122:123], off
	v_cmp_gt_u32_e32 vcc, 64, v140
	s_and_b64 s[36:37], s[18:19], vcc
	s_and_b64 s[56:57], s[36:37], s[20:21]
	v_mov_b64_e32 v[122:123], s[30:31]
	s_and_saveexec_b64 s[36:37], s[56:57]
	v_or_b32_e32 v122, s53, v140
	v_lshl_add_u32 v122, v122, 6, v135
	v_ashrrev_i32_e32 v123, 31, v122
	v_lshlrev_b64 v[122:123], 7, v[122:123]
	v_lshl_add_u64 v[122:123], v[120:121], 0, v[122:123]
	s_or_b64 exec, exec, s[36:37]
	s_add_i32 s36, s55, s46
	v_add_u32_e32 v140, s36, v1
	s_nop 0
	v_readfirstlane_b32 s36, v140
	s_mov_b32 m0, s36
	v_add_u32_e32 v140, s54, v136
	global_load_lds_dwordx4 v[122:123], off
	v_cmp_gt_u32_e32 vcc, 64, v140
	s_and_b64 s[36:37], s[22:23], vcc
	s_and_b64 s[56:57], s[36:37], s[24:25]
	v_mov_b64_e32 v[122:123], s[30:31]
	s_and_saveexec_b64 s[36:37], s[56:57]
	s_cbranch_execz .Lc3_ptail3
	v_or_b32_e32 v122, s53, v140
	v_lshl_add_u32 v122, v122, 6, v137
	v_ashrrev_i32_e32 v123, 31, v122
	v_lshlrev_b64 v[122:123], 7, v[122:123]
	v_lshl_add_u64 v[122:123], v[120:121], 0, v[122:123]
	s_branch .Lc3_ptail3
.Lc3_ptail3:
	s_or_b64 exec, exec, s[36:37]
	s_add_i32 s55, s55, s48
	v_add_u32_e32 v140, s55, v1
	s_add_i32 s51, s51, 1
	v_readfirstlane_b32 s36, v140
	s_mov_b32 m0, s36
	s_mov_b64 s[36:37], -1
	global_load_lds_dwordx4 v[122:123], off
	s_add_i32 s66, s66, 9
	s_cmp_gt_u32 s51, 3
	s_cselect_b32 s66, 0x3e8, s66
	s_mov_b32 s67, 2
.Lc3_np3:
	s_cmp_eq_u32 s67, 0
	s_cbranch_scc1 .Lc3_w2_4
	s_waitcnt vmcnt(8)
	s_sub_i32 s67, s67, 1
	s_branch .Lc3_bar_4

.Lc3_bar_4:
	s_barrier
	s_waitcnt lgkmcnt(5)
	v_mfma_f32_16x16x32_f16 v[110:113], v[66:69], v[78:81], v[110:113]
	ds_read_b128 v[140:143], v172
	s_waitcnt lgkmcnt(5)
	v_mfma_f32_16x16x32_f16 v[106:109], v[70:73], v[78:81], v[106:109]
	v_xor_b32_e32 v174, 64, v139
	s_cmp_eq_u32 s61, 2
	s_cselect_b32 s79, 6, 0
	s_add_i32 s79, s79, s62
	s_add_i32 s79, s79, 4
	s_lshl_b32 s68, s79, 16
	v_mfma_f32_16x16x32_f16 v[62:65], v[66:69], v[74:77], v[62:65]
	ds_read_b128 v[144:147], v172 offset:2048
	v_lshl_add_u64 v[176:177], v[118:119], 0, s[68:69]
	s_add_i32 s70, s49, 0xc000
	s_and_b32 s70, s70, 0xc000
	s_add_i32 s70, s70, s50
	v_mfma_f32_16x16x32_f16 v[58:61], v[70:73], v[74:77], v[58:61]
	s_mov_b32 m0, s70
	s_add_i32 s71, s49, 0x4000
	global_load_lds_dwordx4 v[176:177], off
	s_waitcnt lgkmcnt(5)
	v_mfma_f32_16x16x32_f16 v[46:49], v[66:69], v[82:85], v[46:49]
	ds_read_b128 v[156:159], v174
	v_mfma_f32_16x16x32_f16 v[42:45], v[70:73], v[82:85], v[42:45]
	s_and_b32 s71, s71, 0xc000
	s_add_i32 s72, s70, 0x400
	v_lshl_add_u64 v[178:179], v[176:177], 0, s[34:35]
	s_waitcnt lgkmcnt(5)
	v_mfma_f32_16x16x32_f16 v[34:37], v[66:69], v[86:89], v[34:37]
	ds_read_b128 v[160:163], v174 offset:2048
	v_mfma_f32_16x16x32_f16 v[30:33], v[70:73], v[86:89], v[30:33]
	v_add_u32_e32 v173, s71, v124
	s_mov_b32 s76, s61
	s_mov_b32 s77, s64
	s_waitcnt lgkmcnt(5)
	v_mfma_f32_16x16x32_f16 v[102:105], v[94:97], v[78:81], v[102:105]
	s_waitcnt lgkmcnt(4)
	v_mfma_f32_16x16x32_f16 v[90:93], v[98:101], v[78:81], v[90:93]
	s_add_i32 s78, s76, 102
	v_mfma_f32_16x16x32_f16 v[54:57], v[94:97], v[74:77], v[54:57]
	v_mfma_f32_16x16x32_f16 v[50:53], v[98:101], v[74:77], v[50:53]
	v_add_u32_e32 v180, s78, v116
	v_mfma_f32_16x16x32_f16 v[38:41], v[94:97], v[82:85], v[38:41]
	ds_read_b128 v[164:167], v172 offset:4096
	v_mfma_f32_16x16x32_f16 v[18:21], v[98:101], v[82:85], v[18:21]
	v_bitop3_b32 v181, v180, v115, 6 bitop3:0x6c
	v_lshl_add_u32 v180, v180, 7, s77
	v_mfma_f32_16x16x32_f16 v[26:29], v[94:97], v[86:89], v[26:29]
	ds_read_b128 v[168:171], v172 offset:6144
	v_mfma_f32_16x16x32_f16 v[22:25], v[98:101], v[86:89], v[22:25]
	v_lshl_or_b32 v139, v181, 4, v180
	v_add_u32_e32 v172, s71, v125
	s_waitcnt lgkmcnt(5)
	v_mfma_f32_16x16x32_f16 v[110:113], v[140:143], v[148:151], v[110:113]
	ds_read_b128 v[66:69], v173
	s_waitcnt lgkmcnt(5)
	v_mfma_f32_16x16x32_f16 v[106:109], v[144:147], v[148:151], v[106:109]
	s_mov_b32 m0, s72
	s_addk_i32 s49, 0x4000
	global_load_lds_dwordx4 v[178:179], off
	v_mfma_f32_16x16x32_f16 v[62:65], v[140:143], v[152:155], v[62:65]
	ds_read_b128 v[70:73], v173 offset:2048
	v_mfma_f32_16x16x32_f16 v[58:61], v[144:147], v[152:155], v[58:61]
	s_waitcnt lgkmcnt(5)
	v_mfma_f32_16x16x32_f16 v[46:49], v[140:143], v[156:159], v[46:49]
	ds_read_b128 v[78:81], v139
	v_mfma_f32_16x16x32_f16 v[42:45], v[144:147], v[156:159], v[42:45]
	s_waitcnt lgkmcnt(5)
	v_mfma_f32_16x16x32_f16 v[34:37], v[140:143], v[160:163], v[34:37]
	ds_read_b128 v[74:77], v139 offset:2048
	v_mfma_f32_16x16x32_f16 v[30:33], v[144:147], v[160:163], v[30:33]
	s_waitcnt lgkmcnt(5)
	v_mfma_f32_16x16x32_f16 v[102:105], v[164:167], v[148:151], v[102:105]
	s_waitcnt lgkmcnt(4)
	v_mfma_f32_16x16x32_f16 v[90:93], v[168:171], v[148:151], v[90:93]
	v_mfma_f32_16x16x32_f16 v[54:57], v[164:167], v[152:155], v[54:57]
	v_mfma_f32_16x16x32_f16 v[50:53], v[168:171], v[152:155], v[50:53]
	s_add_i32 s60, s60, 1
	v_mfma_f32_16x16x32_f16 v[38:41], v[164:167], v[156:159], v[38:41]
	ds_read_b128 v[94:97], v173 offset:4096
	v_mfma_f32_16x16x32_f16 v[18:21], v[168:171], v[156:159], v[18:21]
	v_mfma_f32_16x16x32_f16 v[26:29], v[164:167], v[160:163], v[26:29]
	ds_read_b128 v[98:101], v173 offset:6144
	v_mfma_f32_16x16x32_f16 v[22:25], v[168:171], v[160:163], v[22:25]
	s_cmp_eq_u32 s67, 0
	s_cbranch_scc1 .Lc3_w2_5
	s_waitcnt vmcnt(8)
	s_sub_i32 s67, s67, 1
	s_branch .Lc3_bar_5

.Lc3_bar_5:
	s_barrier
	s_waitcnt lgkmcnt(5)
	v_mfma_f32_16x16x32_f16 v[110:113], v[66:69], v[82:85], v[110:113]
	ds_read_b128 v[140:143], v172
	s_waitcnt lgkmcnt(5)
	v_mfma_f32_16x16x32_f16 v[106:109], v[70:73], v[82:85], v[106:109]
	v_xor_b32_e32 v174, 64, v139
	s_cmp_eq_u32 s61, 2
	s_cselect_b32 s79, 6, 0
	s_add_i32 s79, s79, s62
	s_add_i32 s79, s79, 7
	s_lshl_b32 s68, s79, 16
	v_mfma_f32_16x16x32_f16 v[62:65], v[66:69], v[86:89], v[62:65]
	ds_read_b128 v[144:147], v172 offset:2048
	v_lshl_add_u64 v[176:177], v[118:119], 0, s[68:69]
	s_add_i32 s70, s49, 0xc000
	s_and_b32 s70, s70, 0xc000
	s_add_i32 s70, s70, s50
	v_mfma_f32_16x16x32_f16 v[58:61], v[70:73], v[86:89], v[58:61]
	s_mov_b32 m0, s70
	s_add_i32 s71, s49, 0x4000
	global_load_lds_dwordx4 v[176:177], off
	s_waitcnt lgkmcnt(5)
	v_mfma_f32_16x16x32_f16 v[46:49], v[66:69], v[78:81], v[46:49]
	ds_read_b128 v[148:151], v174
	v_mfma_f32_16x16x32_f16 v[42:45], v[70:73], v[78:81], v[42:45]
	s_and_b32 s71, s71, 0xc000
	s_add_i32 s72, s70, 0x400
	v_lshl_add_u64 v[178:179], v[176:177], 0, s[34:35]
	s_waitcnt lgkmcnt(5)
	v_mfma_f32_16x16x32_f16 v[34:37], v[66:69], v[74:77], v[34:37]
	ds_read_b128 v[152:155], v174 offset:2048
	v_mfma_f32_16x16x32_f16 v[30:33], v[70:73], v[74:77], v[30:33]
	v_add_u32_e32 v173, s71, v124
	s_add_i32 s76, s61, 1
	s_cmp_eq_u32 s61, 2
	s_cselect_b32 s76, 0, s76
	s_cselect_b32 s77, 0xc000, 0
	s_xor_b32 s77, s77, s64
	s_waitcnt lgkmcnt(5)
	v_mfma_f32_16x16x32_f16 v[102:105], v[94:97], v[82:85], v[102:105]
	s_waitcnt lgkmcnt(4)
	v_mfma_f32_16x16x32_f16 v[90:93], v[98:101], v[82:85], v[90:93]
	s_add_i32 s78, s76, 34
	v_mfma_f32_16x16x32_f16 v[54:57], v[94:97], v[86:89], v[54:57]
	v_mfma_f32_16x16x32_f16 v[50:53], v[98:101], v[86:89], v[50:53]
	v_add_u32_e32 v180, s78, v116
	v_mfma_f32_16x16x32_f16 v[38:41], v[94:97], v[78:81], v[38:41]
	ds_read_b128 v[164:167], v172 offset:4096
	v_mfma_f32_16x16x32_f16 v[18:21], v[98:101], v[78:81], v[18:21]
	v_bitop3_b32 v181, v180, v115, 6 bitop3:0x6c
	v_lshl_add_u32 v180, v180, 7, s77
	v_mfma_f32_16x16x32_f16 v[26:29], v[94:97], v[74:77], v[26:29]
	ds_read_b128 v[168:171], v172 offset:6144
	v_mfma_f32_16x16x32_f16 v[22:25], v[98:101], v[74:77], v[22:25]
	v_lshl_or_b32 v139, v181, 4, v180
	v_add_u32_e32 v172, s71, v125
	s_waitcnt lgkmcnt(5)
	v_mfma_f32_16x16x32_f16 v[110:113], v[140:143], v[156:159], v[110:113]
	ds_read_b128 v[66:69], v173
	s_waitcnt lgkmcnt(5)
	v_mfma_f32_16x16x32_f16 v[106:109], v[144:147], v[156:159], v[106:109]
	s_mov_b32 m0, s72
	s_addk_i32 s49, 0x4000
	global_load_lds_dwordx4 v[178:179], off
	v_mfma_f32_16x16x32_f16 v[62:65], v[140:143], v[160:163], v[62:65]
	ds_read_b128 v[70:73], v173 offset:2048
	v_mfma_f32_16x16x32_f16 v[58:61], v[144:147], v[160:163], v[58:61]
	s_sub_i32 s78, s78, 34
	v_add_u32_e32 v180, s78, v116
	s_waitcnt lgkmcnt(5)
	v_mfma_f32_16x16x32_f16 v[46:49], v[140:143], v[148:151], v[46:49]
	ds_read_b128 v[82:85], v139
	v_mfma_f32_16x16x32_f16 v[42:45], v[144:147], v[148:151], v[42:45]
	v_bitop3_b32 v181, v180, v115, 6 bitop3:0x6c
	v_lshl_add_u32 v180, v180, 7, s77
	s_waitcnt lgkmcnt(5)
	v_mfma_f32_16x16x32_f16 v[34:37], v[140:143], v[152:155], v[34:37]
	ds_read_b128 v[86:89], v139 offset:2048
	v_mfma_f32_16x16x32_f16 v[30:33], v[144:147], v[152:155], v[30:33]
	v_lshl_or_b32 v138, v181, 4, v180
	s_waitcnt lgkmcnt(5)
	v_mfma_f32_16x16x32_f16 v[102:105], v[164:167], v[156:159], v[102:105]
	ds_read_b128 v[78:81], v138
	s_waitcnt lgkmcnt(5)
	v_mfma_f32_16x16x32_f16 v[90:93], v[168:171], v[156:159], v[90:93]
	v_mfma_f32_16x16x32_f16 v[54:57], v[164:167], v[160:163], v[54:57]
	ds_read_b128 v[74:77], v138 offset:2048
	v_mfma_f32_16x16x32_f16 v[50:53], v[168:171], v[160:163], v[50:53]
	s_add_i32 s60, s60, 1
	s_cmp_eq_u32 s61, 2
	s_cselect_b32 s79, 7, 1
	s_add_i32 s62, s62, s79
	s_mov_b32 s61, s76
	s_mov_b32 s64, s77
	v_mfma_f32_16x16x32_f16 v[38:41], v[164:167], v[148:151], v[38:41]
	ds_read_b128 v[94:97], v173 offset:4096
	v_mfma_f32_16x16x32_f16 v[18:21], v[168:171], v[148:151], v[18:21]
	v_mfma_f32_16x16x32_f16 v[26:29], v[164:167], v[152:155], v[26:29]
	ds_read_b128 v[98:101], v173 offset:6144
	v_mfma_f32_16x16x32_f16 v[22:25], v[168:171], v[152:155], v[22:25]
	s_cmp_eq_u32 s60, 36
	s_cbranch_scc0 .Lc3_loop
